# union13 + widen K-loop tail: next-unit staging block moved out of line, common path falls through
# speedup vs baseline: 1.0034x; 1.0001x over previous
; #define PG8_STAGE(bufoff, gbase, voff) do { _Pragma("unroll") for (int _i = 0; _i < 2; ++_i) \
;         __builtin_amdgcn_global_load_lds((const unsigned*)((const char*)(gbase) + (voff)[_i]), (PG8_LAS unsigned*)(lds + (bufoff) + ldsw + _i * 8192), 16, 0, 0); } while (0)
; #define PG8_LDA(dst, b, h) do { _Pragma("unroll") for (int m = 0; m < 4; ++m) _Pragma("unroll") for (int k = 0; k < 2; ++k) dst[m][k] = *(const PG8_LAS bf16x8*)(lds + PG8_SA(b, h) + aoff + m * 2048 + k * 1024); } while (0)
; #define PG8_MMA(ai, bj, At, Bt) do { __builtin_amdgcn_s_setprio(1); _Pragma("unroll") for (int m = 0; m < 4; ++m) _Pragma("unroll") for (int n = 0; n < 2; ++n) _Pragma("unroll") for (int k = 0; k < 2; ++k) \
;         acc[ai][bj][m][n] = mma16(Bt[n][k], At[m][k], acc[ai][bj][m][n]); __builtin_amdgcn_s_setprio(0); } while (0)
; #define PG8_WAIT_V(n) asm volatile("s_waitcnt vmcnt(" #n ")" ::: "memory")
; #define PG8_WAIT_VN(n) asm volatile("s_waitcnt vmcnt(%0)" :: "n"(n) : "memory")
; #define PG8_WAIT_L(n) asm volatile("s_waitcnt lgkmcnt(" #n ")" ::: "memory")
; #define PG8_BAR __builtin_amdgcn_s_barrier()
; #define PG8_SCHED __builtin_amdgcn_sched_barrier(0)
; template <class Epi, class Sched, bool ALIGN_EPI = false, bool SP2 = false>
; __device__ __forceinline__ void gemm_phase(PG8_LAS unsigned char* lds, const Gemm g, const Sched& S, const Epi& E, Stopwatch& sw) {
;     ...
;             if (relax) PG8_WAIT_VN(8 + Epi::NST); else PG8_WAIT_V(8); PG8_WAIT_L(0); PG8_BAR; PG8_MMA(0, 0, At, B0); PG8_MMA(0, 1, At, B1); PG8_BAR; PG8_SCHED;
;             PG8_LDA(At, 1, 1); PG8_STAGE(PG8_SB(1, 0), b3, voffB); PG8_STAGE(PG8_SB(1, 1), b3 + hstep, voffB); PG8_STAGE(PG8_SA(1, 0), a3, voffA);
;             PG8_WAIT_V(8); PG8_WAIT_L(0); PG8_BAR; PG8_MMA(1, 0, At, B0); PG8_MMA(1, 1, At, B1); PG8_BAR; PG8_SCHED;
;             if (last && has_next) PG8_STAGE(PG8_SA(1, 1), a3 + hstep, voffA);
.LBB0_786:
	s_waitcnt lgkmcnt(0)
	s_and_b64 s[42:43], s[40:41], s[62:63]
	s_barrier
	s_setprio 1
	s_waitcnt lgkmcnt(0)
	v_mfma_f32_16x16x32_bf16 v[130:133], v[150:153], v[190:193], v[130:133]
	v_mfma_f32_16x16x32_bf16 v[126:129], v[158:161], v[190:193], v[126:129]
	v_mfma_f32_16x16x32_bf16 v[114:117], v[150:153], v[182:185], v[114:117]
	v_mfma_f32_16x16x32_bf16 v[110:113], v[158:161], v[182:185], v[110:113]
	v_mfma_f32_16x16x32_bf16 v[98:101], v[150:153], v[174:177], v[98:101]
	v_mfma_f32_16x16x32_bf16 v[94:97], v[158:161], v[174:177], v[94:97]
	v_mfma_f32_16x16x32_bf16 v[82:85], v[150:153], v[166:169], v[82:85]
	v_mfma_f32_16x16x32_bf16 v[78:81], v[158:161], v[166:169], v[78:81]
	v_mfma_f32_16x16x32_bf16 v[130:133], v[154:157], v[194:197], v[130:133]
	v_mfma_f32_16x16x32_bf16 v[126:129], v[162:165], v[194:197], v[126:129]
	v_mfma_f32_16x16x32_bf16 v[114:117], v[154:157], v[186:189], v[114:117]
	v_mfma_f32_16x16x32_bf16 v[110:113], v[162:165], v[186:189], v[110:113]
	v_mfma_f32_16x16x32_bf16 v[98:101], v[154:157], v[178:181], v[98:101]
	v_mfma_f32_16x16x32_bf16 v[94:97], v[162:165], v[178:181], v[94:97]
	v_mfma_f32_16x16x32_bf16 v[82:85], v[154:157], v[170:173], v[82:85]
	v_mfma_f32_16x16x32_bf16 v[78:81], v[162:165], v[170:173], v[78:81]
	v_mfma_f32_16x16x32_bf16 v[122:125], v[134:137], v[190:193], v[122:125]
	v_mfma_f32_16x16x32_bf16 v[118:121], v[142:145], v[190:193], v[118:121]
	v_mfma_f32_16x16x32_bf16 v[106:109], v[134:137], v[182:185], v[106:109]
	v_mfma_f32_16x16x32_bf16 v[102:105], v[142:145], v[182:185], v[102:105]
	v_mfma_f32_16x16x32_bf16 v[90:93], v[134:137], v[174:177], v[90:93]
	v_mfma_f32_16x16x32_bf16 v[86:89], v[142:145], v[174:177], v[86:89]
	v_mfma_f32_16x16x32_bf16 v[74:77], v[134:137], v[166:169], v[74:77]
	v_mfma_f32_16x16x32_bf16 v[70:73], v[142:145], v[166:169], v[70:73]
	v_mfma_f32_16x16x32_bf16 v[122:125], v[138:141], v[194:197], v[122:125]
	v_mfma_f32_16x16x32_bf16 v[118:121], v[146:149], v[194:197], v[118:121]
	v_mfma_f32_16x16x32_bf16 v[106:109], v[138:141], v[186:189], v[106:109]
	v_mfma_f32_16x16x32_bf16 v[102:105], v[146:149], v[186:189], v[102:105]
	v_mfma_f32_16x16x32_bf16 v[90:93], v[138:141], v[178:181], v[90:93]
	v_mfma_f32_16x16x32_bf16 v[86:89], v[146:149], v[178:181], v[86:89]
	v_mfma_f32_16x16x32_bf16 v[74:77], v[138:141], v[170:173], v[74:77]
	v_mfma_f32_16x16x32_bf16 v[70:73], v[146:149], v[170:173], v[70:73]
	s_setprio 0
	s_barrier
	s_mov_b32 m0, s79
	v_lshl_add_u64 v[8:9], v[230:231], 0, s[20:21]
	s_add_u32 s60, s60, 0xc0080
	ds_read_b128 v[166:169], v249 offset:49152
	ds_read_b128 v[170:173], v249 offset:50176
	ds_read_b128 v[174:177], v249 offset:51200
	ds_read_b128 v[178:181], v249 offset:52224
	ds_read_b128 v[182:185], v249 offset:53248
	ds_read_b128 v[186:189], v249 offset:54272
	ds_read_b128 v[190:193], v249 offset:55296
	ds_read_b128 v[194:197], v249 offset:56320
	global_load_lds_dwordx4 v[8:9], off
	v_lshl_add_u64 v[8:9], v[232:233], 0, s[20:21]
	s_mov_b32 m0, s80
	s_addc_u32 s61, s61, 0
	global_load_lds_dwordx4 v[8:9], off
	v_lshl_add_u64 v[8:9], s[60:61], 0, v[206:207]
	s_mov_b32 m0, s94
	s_nop 0
	global_load_lds_dwordx4 v[8:9], off
	v_lshl_add_u64 v[8:9], s[60:61], 0, v[202:203]
	s_mov_b32 m0, s95
	s_nop 0
	global_load_lds_dwordx4 v[8:9], off
	v_lshl_add_u64 v[8:9], v[234:235], 0, s[20:21]
	s_mov_b32 m0, s81
	s_nop 0
	global_load_lds_dwordx4 v[8:9], off
	v_lshl_add_u64 v[8:9], v[236:237], 0, s[20:21]
	s_mov_b32 m0, s90
	s_nop 0
	global_load_lds_dwordx4 v[8:9], off
	s_waitcnt vmcnt(8)
	s_waitcnt lgkmcnt(0)
	s_barrier
	s_setprio 1
	s_waitcnt lgkmcnt(0)
	v_mfma_f32_16x16x32_bf16 v[66:69], v[150:153], v[166:169], v[66:69]
	v_mfma_f32_16x16x32_bf16 v[62:65], v[158:161], v[166:169], v[62:65]
	v_mfma_f32_16x16x32_bf16 v[50:53], v[150:153], v[174:177], v[50:53]
	v_mfma_f32_16x16x32_bf16 v[46:49], v[158:161], v[174:177], v[46:49]
	v_mfma_f32_16x16x32_bf16 v[34:37], v[150:153], v[182:185], v[34:37]
	v_mfma_f32_16x16x32_bf16 v[30:33], v[158:161], v[182:185], v[30:33]
	v_mfma_f32_16x16x32_bf16 v[18:21], v[150:153], v[190:193], v[18:21]
	v_mfma_f32_16x16x32_bf16 v[14:17], v[158:161], v[190:193], v[14:17]
	v_mfma_f32_16x16x32_bf16 v[66:69], v[154:157], v[170:173], v[66:69]
	v_mfma_f32_16x16x32_bf16 v[62:65], v[162:165], v[170:173], v[62:65]
	v_mfma_f32_16x16x32_bf16 v[50:53], v[154:157], v[178:181], v[50:53]
	v_mfma_f32_16x16x32_bf16 v[46:49], v[162:165], v[178:181], v[46:49]
	v_mfma_f32_16x16x32_bf16 v[34:37], v[154:157], v[186:189], v[34:37]
	v_mfma_f32_16x16x32_bf16 v[30:33], v[162:165], v[186:189], v[30:33]
	v_mfma_f32_16x16x32_bf16 v[18:21], v[154:157], v[194:197], v[18:21]
	v_mfma_f32_16x16x32_bf16 v[14:17], v[162:165], v[194:197], v[14:17]
	v_mfma_f32_16x16x32_bf16 v[58:61], v[134:137], v[166:169], v[58:61]
	v_mfma_f32_16x16x32_bf16 v[54:57], v[142:145], v[166:169], v[54:57]
	v_mfma_f32_16x16x32_bf16 v[42:45], v[134:137], v[174:177], v[42:45]
	v_mfma_f32_16x16x32_bf16 v[38:41], v[142:145], v[174:177], v[38:41]
	v_mfma_f32_16x16x32_bf16 v[26:29], v[134:137], v[182:185], v[26:29]
	v_mfma_f32_16x16x32_bf16 v[22:25], v[142:145], v[182:185], v[22:25]
	v_mfma_f32_16x16x32_bf16 v[8:11], v[134:137], v[190:193], v[10:13]
	v_mfma_f32_16x16x32_bf16 v[4:7], v[142:145], v[190:193], v[4:7]
	v_mfma_f32_16x16x32_bf16 v[58:61], v[138:141], v[170:173], v[58:61]
	v_mfma_f32_16x16x32_bf16 v[54:57], v[146:149], v[170:173], v[54:57]
	v_mfma_f32_16x16x32_bf16 v[42:45], v[138:141], v[178:181], v[42:45]
	v_mfma_f32_16x16x32_bf16 v[38:41], v[146:149], v[178:181], v[38:41]
	v_mfma_f32_16x16x32_bf16 v[26:29], v[138:141], v[186:189], v[26:29]
	v_mfma_f32_16x16x32_bf16 v[22:25], v[146:149], v[186:189], v[22:25]
	v_mfma_f32_16x16x32_bf16 v[10:13], v[138:141], v[194:197], v[8:11]
	v_mfma_f32_16x16x32_bf16 v[6:9], v[146:149], v[194:197], v[4:7]
	s_setprio 0
	s_barrier
	s_andn2_b64 vcc, exec, s[42:43]
	s_cbranch_vccz .Lw_stage

; #define PG8_STAGE(bufoff, gbase, voff) do { _Pragma("unroll") for (int _i = 0; _i < 2; ++_i) \
;         __builtin_amdgcn_global_load_lds((const unsigned*)((const char*)(gbase) + (voff)[_i]), (PG8_LAS unsigned*)(lds + (bufoff) + ldsw + _i * 8192), 16, 0, 0); } while (0)
; template <class Epi, class Sched, bool ALIGN_EPI = false, bool SP2 = false>
; __device__ __forceinline__ void gemm_phase(PG8_LAS unsigned char* lds, const Gemm g, const Sched& S, const Epi& E, Stopwatch& sw) {
;     ...
;             if (last && has_next) PG8_STAGE(PG8_SA(1, 1), a3 + hstep, voffA);
.Lw_stage:
	s_add_i32 m0, s18, 0xc000
	s_nop 0
	global_load_lds_dwordx4 v[220:221], off
	s_add_i32 m0, s18, 0xe000
	s_nop 0
	global_load_lds_dwordx4 v[222:223], off
	s_branch .LBB0_788
